# speedup vs baseline: 1.0229x; 1.0004x over previous
.LBB4_11:
	s_and_b32 s14, s15, 1
	global_load_dwordx4 v[112:115], v128, s[8:9]
	global_load_dwordx4 v[116:119], v204, s[8:9]
	global_load_dwordx4 v[120:123], v128, s[0:1]
	global_load_dwordx4 v[124:127], v204, s[0:1]
	s_add_i32 s15, s15, 1
	s_mul_i32 s18, s14, 0x2400
	v_add_u32_e32 v202, s18, v167
	ds_read_b128 v[80:83], v202
	ds_read_b128 v[190:193], v202 offset:32
	ds_read_b128 v[194:197], v202 offset:4608
	ds_read_b128 v[198:201], v202 offset:4640
	s_waitcnt lgkmcnt(3)
	v_mfma_f32_32x32x16_f16 v[64:79], v[108:111], v[80:83], v[48:63]
	s_waitcnt lgkmcnt(1)
	v_mfma_f32_32x32x16_f16 v[80:95], v[108:111], v[194:197], v[48:63]
	v_mfma_f32_32x32x16_f16 v[64:79], v[104:107], v[190:193], v[64:79]
	ds_read_b128 v[190:193], v202 offset:64
	ds_read_b128 v[194:197], v202 offset:96
	s_waitcnt lgkmcnt(2)
	v_mfma_f32_32x32x16_f16 v[80:95], v[104:107], v[198:201], v[80:95]
	s_waitcnt lgkmcnt(1)
	v_mfma_f32_32x32x16_f16 v[64:79], v[100:103], v[190:193], v[64:79]
	ds_read_b128 v[190:193], v202 offset:4672
	ds_read_b128 v[198:201], v202 offset:4704
	s_waitcnt lgkmcnt(1)
	v_mfma_f32_32x32x16_f16 v[80:95], v[100:103], v[190:193], v[80:95]
	v_mfma_f32_32x32x16_f16 v[64:79], v[96:99], v[194:197], v[64:79]
	s_waitcnt lgkmcnt(0)
	v_mfma_f32_32x32x16_f16 v[80:95], v[96:99], v[198:201], v[80:95]
	s_setprio 2
	s_nop 8
	v_exp_f32_e32 v192, v64
	s_nop 0
	v_exp_f32_e32 v80, v80
	v_exp_f32_e32 v193, v65
	v_exp_f32_e32 v81, v81
	v_mul_f32_e32 v64, v192, v183
	v_exp_f32_e32 v66, v66
	global_store_dword v132, v64, s[42:43] offset:-128
	v_mul_f32_e32 v64, v80, v183
	v_exp_f32_e32 v82, v82
	global_store_dword v132, v64, s[42:43]
	v_mul_f32_e32 v190, v193, v182
	v_exp_f32_e32 v67, v67
	global_store_dword v136, v190, s[42:43] offset:-128
	v_mul_f32_e32 v190, v81, v182
	v_exp_f32_e32 v83, v83
	global_store_dword v136, v190, s[42:43]
	v_mul_f32_e32 v190, v66, v181
	global_store_dword v140, v190, s[42:43] offset:-128
	v_mul_f32_e32 v190, v82, v181
	global_store_dword v140, v190, s[42:43]
	v_mul_f32_e32 v190, v67, v180
	global_store_dword v144, v190, s[42:43] offset:-128
	v_mul_f32_e32 v190, v83, v180
	global_store_dword v144, v190, s[42:43]
	v_exp_f32_e32 v190, v68
	v_cvt_pk_f16_f32 v65, v66, v67
	v_cvt_pk_f16_f32 v67, v82, v83
	v_exp_f32_e32 v82, v84
	v_cvt_pk_f16_f32 v66, v80, v81
	v_mul_f32_e32 v68, v190, v179
	global_store_dword v148, v68, s[42:43] offset:-128
	v_exp_f32_e32 v83, v69
	v_mul_f32_e32 v68, v82, v179
	global_store_dword v148, v68, s[42:43]
	v_exp_f32_e32 v80, v85
	v_mul_f32_e32 v81, v83, v178
	global_store_dword v152, v81, s[42:43] offset:-128
	v_exp_f32_e32 v70, v70
	v_mul_f32_e32 v81, v80, v178
	global_store_dword v152, v81, s[42:43]
	v_exp_f32_e32 v81, v86
	v_mul_f32_e32 v84, v70, v177
	global_store_dword v156, v84, s[42:43] offset:-128
	v_exp_f32_e32 v71, v71
	v_mul_f32_e32 v84, v81, v177
	global_store_dword v156, v84, s[42:43]
	v_exp_f32_e32 v84, v87
	v_mul_f32_e32 v85, v71, v176
	global_store_dword v160, v85, s[42:43] offset:-128
	v_mul_f32_e32 v85, v84, v176
	v_cvt_pk_f16_f32 v64, v192, v193
	global_store_dword v160, v85, s[42:43]
	v_cvt_pk_f16_f32 v69, v70, v71
	v_cvt_pk_f16_f32 v68, v190, v83
	v_exp_f32_e32 v72, v72
	v_cvt_pk_f16_f32 v71, v81, v84
	v_cvt_pk_f16_f32 v70, v82, v80
	ds_write2_b64 v187, v[64:65], v[68:69] offset1:2
	ds_write2_b64 v131, v[66:67], v[70:71] offset0:32 offset1:34
	v_exp_f32_e32 v66, v88
	v_mul_f32_e32 v67, v72, v175
	global_store_dword v162, v67, s[42:43]
	v_exp_f32_e32 v67, v73
	v_mul_f32_e32 v68, v66, v175
	global_store_dword v162, v68, s[42:43] offset:128
	v_exp_f32_e32 v68, v89
	v_mul_f32_e32 v69, v67, v174
	global_store_dword v158, v69, s[42:43]
	v_exp_f32_e32 v69, v74
	v_mul_f32_e32 v70, v68, v174
	global_store_dword v158, v70, s[42:43] offset:128
	v_exp_f32_e32 v70, v90
	v_mul_f32_e32 v71, v69, v173
	global_store_dword v154, v71, s[42:43]
	v_exp_f32_e32 v71, v75
	v_mul_f32_e32 v73, v70, v173
	global_store_dword v154, v73, s[42:43] offset:128
	v_exp_f32_e32 v73, v91
	v_mul_f32_e32 v74, v71, v172
	global_store_dword v150, v74, s[42:43]
	v_mul_f32_e32 v74, v73, v172
	global_store_dword v150, v74, s[42:43] offset:128
	v_cvt_pk_f16_f32 v65, v69, v71
	v_exp_f32_e32 v71, v76
	v_cvt_pk_f16_f32 v64, v72, v67
	v_cvt_pk_f16_f32 v67, v70, v73
	v_exp_f32_e32 v70, v92
	v_cvt_pk_f16_f32 v66, v66, v68
	v_mul_f32_e32 v72, v71, v171
	global_store_dword v146, v72, s[42:43]
	v_exp_f32_e32 v72, v77
	v_mul_f32_e32 v73, v70, v171
	global_store_dword v146, v73, s[42:43] offset:128
	v_exp_f32_e32 v73, v93
	v_mul_f32_e32 v74, v72, v170
	global_store_dword v142, v74, s[42:43]
	v_exp_f32_e32 v74, v78
	v_mul_f32_e32 v75, v73, v170
	global_store_dword v142, v75, s[42:43] offset:128
	v_exp_f32_e32 v75, v94
	v_mul_f32_e32 v76, v74, v169
	global_store_dword v138, v76, s[42:43]
	v_exp_f32_e32 v76, v79
	v_mul_f32_e32 v77, v75, v169
	global_store_dword v138, v77, s[42:43] offset:128
	v_exp_f32_e32 v77, v95
	v_mul_f32_e32 v78, v76, v168
	global_store_dword v134, v78, s[42:43]
	v_mul_f32_e32 v78, v77, v168
	global_store_dword v134, v78, s[42:43] offset:128
	v_cvt_pk_f16_f32 v69, v74, v76
	v_cvt_pk_f16_f32 v68, v71, v72
	v_cvt_pk_f16_f32 v71, v75, v77
	v_cvt_pk_f16_f32 v70, v70, v73
	ds_write2_b64 v187, v[64:65], v[68:69] offset0:4 offset1:6
	ds_write2_b64 v131, v[66:67], v[70:71] offset0:36 offset1:38
	s_setprio 0
	ds_read_b64_tr_b16 v[64:65], v186
	ds_read_b64_tr_b16 v[66:67], v186 offset:288
	s_mul_i32 s18, s14, 0x3000
	v_or_b32_e32 v80, s18, v185
	ds_read_b64_tr_b16 v[68:69], v80
	ds_read_b64_tr_b16 v[70:71], v80 offset:768
	ds_read_b64_tr_b16 v[74:75], v80 offset:832
	ds_read_b64_tr_b16 v[72:73], v80 offset:64
	ds_read_b64_tr_b16 v[76:77], v186 offset:1152
	ds_read_b64_tr_b16 v[78:79], v186 offset:1440
	s_waitcnt lgkmcnt(4)
	v_mfma_f32_32x32x16_f16 v[0:15], v[64:67], v[68:71], v[0:15]
	s_waitcnt lgkmcnt(2)
	v_mfma_f32_32x32x16_f16 v[16:31], v[64:67], v[72:75], v[16:31]
	ds_read_b64_tr_b16 v[64:65], v80 offset:3072
	ds_read_b64_tr_b16 v[66:67], v80 offset:3840
	ds_read_b64_tr_b16 v[70:71], v80 offset:3904
	ds_read_b64_tr_b16 v[68:69], v80 offset:3136
	s_waitcnt lgkmcnt(2)
	v_mfma_f32_32x32x16_f16 v[0:15], v[76:79], v[64:67], v[0:15]
	s_waitcnt lgkmcnt(0)
	v_mfma_f32_32x32x16_f16 v[16:31], v[76:79], v[68:71], v[16:31]
	ds_read_b64_tr_b16 v[64:65], v186 offset:2304
	ds_read_b64_tr_b16 v[66:67], v186 offset:2592
	ds_read_b64_tr_b16 v[68:69], v80 offset:6144
	ds_read_b64_tr_b16 v[70:71], v80 offset:6912
	ds_read_b64_tr_b16 v[74:75], v80 offset:6976
	ds_read_b64_tr_b16 v[72:73], v80 offset:6208
	ds_read_b64_tr_b16 v[76:77], v186 offset:3456
	ds_read_b64_tr_b16 v[78:79], v186 offset:3744
	s_waitcnt lgkmcnt(4)
	v_mfma_f32_32x32x16_f16 v[0:15], v[64:67], v[68:71], v[0:15]
	s_waitcnt lgkmcnt(2)
	v_mfma_f32_32x32x16_f16 v[16:31], v[64:67], v[72:75], v[16:31]
	ds_read_b64_tr_b16 v[64:65], v80 offset:9216
	ds_read_b64_tr_b16 v[66:67], v80 offset:9984
	ds_read_b64_tr_b16 v[70:71], v80 offset:10048
	ds_read_b64_tr_b16 v[68:69], v80 offset:9280
	s_waitcnt lgkmcnt(2)
	v_mfma_f32_32x32x16_f16 v[0:15], v[76:79], v[64:67], v[0:15]
	s_waitcnt lgkmcnt(0)
	v_mfma_f32_32x32x16_f16 v[16:31], v[76:79], v[68:71], v[16:31]
	s_xor_b32 s14, s14, 1
	s_mul_i32 s18, s14, 0x3000
	s_mulk_i32 s14, 0x2400
	s_addk_i32 s14, 0x6000
	s_add_u32 s10, s10, 0x100
	s_addc_u32 s11, s11, 0
	s_add_u32 s42, s42, 0x100
	s_addc_u32 s43, s43, 0
	s_add_u32 s8, s8, 0x2000
	s_addc_u32 s9, s9, 0
	s_add_u32 s0, s0, 0x2000
	s_addc_u32 s1, s1, 0
	v_lshl_add_u32 v67, v166, 1, s14
	s_cmpk_eq_i32 s10, 0x1f00
	v_lshl_add_u32 v64, v189, 1, s18
	v_lshl_add_u32 v65, v188, 1, s18
	v_lshl_add_u32 v66, v165, 1, s14
	s_waitcnt vmcnt(35)
	ds_write_b128 v67, v[112:115]
	s_waitcnt vmcnt(34)
	ds_write_b128 v66, v[116:119]
	s_waitcnt vmcnt(33)
	ds_write_b128 v65, v[120:123]
	s_waitcnt vmcnt(32)
	ds_write_b128 v64, v[124:127]
	s_waitcnt lgkmcnt(0)
	s_barrier
	s_cbranch_scc0 .LBB4_11
	s_lshl_b64 s[0:1], s[16:17], 13
	s_add_u32 s0, s4, s0
	s_addc_u32 s1, s5, s1
	v_xor_b32_e32 v52, 0x80000000, v34
	v_xor_b32_e32 v51, 0x80000000, v35
	v_xor_b32_e32 v50, 0x80000000, v32
	v_xor_b32_e32 v49, 0x80000000, v33
	ds_read_b128 v[32:35], v167 offset:9216
	v_xor_b32_e32 v59, 0x80000000, v43
	v_xor_b32_e32 v58, 0x80000000, v40
	v_xor_b32_e32 v57, 0x80000000, v41
	v_xor_b32_e32 v56, 0x80000000, v38
	v_xor_b32_e32 v55, 0x80000000, v39
	v_xor_b32_e32 v54, 0x80000000, v36
	v_xor_b32_e32 v53, 0x80000000, v37
	v_xor_b32_e32 v48, 0x80000000, v46
	v_xor_b32_e32 v47, 0x80000000, v47
	v_xor_b32_e32 v46, 0x80000000, v42
	v_xor_b32_e32 v45, 0x80000000, v45
	v_xor_b32_e32 v44, 0x80000000, v44
	ds_read_b128 v[36:39], v167 offset:9248
	s_add_u32 s0, s0, 0x1f00
	s_waitcnt lgkmcnt(1)
	v_mfma_f32_32x32x16_f16 v[60:75], v[108:111], v[32:35], v[44:59]
	ds_read_b128 v[32:35], v167 offset:13824
	ds_read_b128 v[40:43], v167 offset:13856
	s_addc_u32 s1, s1, 0
	s_waitcnt lgkmcnt(1)
	v_mfma_f32_32x32x16_f16 v[44:59], v[108:111], v[32:35], v[44:59]
	v_mfma_f32_32x32x16_f16 v[60:75], v[104:107], v[36:39], v[60:75]
	ds_read_b128 v[32:35], v167 offset:9280
	ds_read_b128 v[36:39], v167 offset:9312
	s_waitcnt lgkmcnt(2)
	v_mfma_f32_32x32x16_f16 v[44:59], v[104:107], v[40:43], v[44:59]
	s_waitcnt lgkmcnt(1)
	v_mfma_f32_32x32x16_f16 v[60:75], v[100:103], v[32:35], v[60:75]
	ds_read_b128 v[32:35], v167 offset:13888
	ds_read_b128 v[40:43], v167 offset:13920
	s_waitcnt lgkmcnt(1)
	v_mfma_f32_32x32x16_f16 v[44:59], v[100:103], v[32:35], v[44:59]
	v_mfma_f32_32x32x16_f16 v[60:75], v[96:99], v[36:39], v[60:75]
	s_waitcnt lgkmcnt(0)
	v_mfma_f32_32x32x16_f16 v[44:59], v[96:99], v[40:43], v[44:59]
	s_setprio 2
	s_nop 8
	v_exp_f32_e32 v32, v60
	s_nop 0
	v_exp_f32_e32 v34, v44
	v_exp_f32_e32 v35, v61
	v_or_b32_e32 v37, 0x2000, v130
	v_mul_f32_e32 v33, v32, v183
	v_mul_f32_e32 v36, v34, v183
	global_store_dword v130, v33, s[0:1]
	global_store_dword v130, v36, s[0:1] offset:128
	v_exp_f32_e32 v36, v45
	v_mul_f32_e32 v33, v35, v182
	global_store_dword v37, v33, s[0:1]
	v_exp_f32_e32 v33, v62
	v_mul_f32_e32 v38, v36, v182
	global_store_dword v37, v38, s[0:1] offset:128
	v_exp_f32_e32 v37, v46
	v_mul_f32_e32 v38, v33, v181
	v_or_b32_e32 v39, 0x4000, v130
	global_store_dword v39, v38, s[0:1]
	v_exp_f32_e32 v38, v63
	v_mul_f32_e32 v40, v37, v181
	global_store_dword v39, v40, s[0:1] offset:128
	v_exp_f32_e32 v39, v47
	v_mul_f32_e32 v40, v38, v180
	v_cvt_pk_f16_f32 v33, v33, v38
	v_exp_f32_e32 v38, v64
	v_or_b32_e32 v41, 0x6000, v130
	global_store_dword v41, v40, s[0:1]
	v_mul_f32_e32 v40, v39, v180
	global_store_dword v41, v40, s[0:1] offset:128
	v_cvt_pk_f16_f32 v32, v32, v35
	v_cvt_pk_f16_f32 v35, v37, v39
	v_cvt_pk_f16_f32 v34, v34, v36
	v_exp_f32_e32 v40, v48
	v_mul_f32_e32 v36, v38, v179
	v_or_b32_e32 v37, 0x10000, v130
	global_store_dword v37, v36, s[0:1]
	v_exp_f32_e32 v36, v65
	v_exp_f32_e32 v41, v49
	v_mul_f32_e32 v39, v40, v179
	global_store_dword v37, v39, s[0:1] offset:128
	v_mul_f32_e32 v37, v36, v178
	v_or_b32_e32 v39, 0x12000, v130
	global_store_dword v39, v37, s[0:1]
	v_exp_f32_e32 v37, v66
	v_mul_f32_e32 v42, v41, v178
	global_store_dword v39, v42, s[0:1] offset:128
	v_exp_f32_e32 v39, v50
	v_mul_f32_e32 v42, v37, v177
	v_or_b32_e32 v43, 0x14000, v130
	global_store_dword v43, v42, s[0:1]
	v_exp_f32_e32 v42, v67
	v_mul_f32_e32 v44, v39, v177
	global_store_dword v43, v44, s[0:1] offset:128
	v_exp_f32_e32 v43, v51
	v_cvt_pk_f16_f32 v37, v37, v42
	v_cvt_pk_f16_f32 v36, v38, v36
	v_cvt_pk_f16_f32 v38, v40, v41
	v_cvt_pk_f16_f32 v39, v39, v43
	ds_write2_b64 v187, v[32:33], v[36:37] offset1:2
	v_exp_f32_e32 v32, v68
	v_add_u32_e32 v40, 0x800, v187
	ds_write2_b64 v40, v[34:35], v[38:39] offset0:32 offset1:34
	v_exp_f32_e32 v34, v52
	v_exp_f32_e32 v36, v69
	v_exp_f32_e32 v37, v53
	v_mul_f32_e32 v33, v32, v175
	v_or_b32_e32 v35, 0x20000, v130
	global_store_dword v35, v33, s[0:1]
	v_mul_f32_e32 v33, v34, v175
	global_store_dword v35, v33, s[0:1] offset:128
	v_mul_f32_e32 v33, v36, v174
	v_or_b32_e32 v35, 0x22000, v130
	global_store_dword v35, v33, s[0:1]
	v_exp_f32_e32 v33, v70
	v_mul_f32_e32 v38, v37, v174
	global_store_dword v35, v38, s[0:1] offset:128
	v_exp_f32_e32 v35, v54
	v_mul_f32_e32 v38, v33, v173
	v_or_b32_e32 v39, 0x24000, v130
	global_store_dword v39, v38, s[0:1]
	v_exp_f32_e32 v38, v71
	v_mul_f32_e32 v41, v35, v173
	global_store_dword v39, v41, s[0:1] offset:128
	v_exp_f32_e32 v39, v55
	v_mul_f32_e32 v44, v42, v176
	v_mul_f32_e32 v41, v38, v172
	v_or_b32_e32 v42, 0x26000, v130
	v_cvt_pk_f16_f32 v32, v32, v36
	v_exp_f32_e32 v36, v72
	global_store_dword v42, v41, s[0:1]
	v_mul_f32_e32 v41, v39, v172
	v_cvt_pk_f16_f32 v33, v33, v38
	v_exp_f32_e32 v38, v56
	global_store_dword v42, v41, s[0:1] offset:128
	v_exp_f32_e32 v41, v73
	v_exp_f32_e32 v42, v57
	v_cvt_pk_f16_f32 v35, v35, v39
	v_cvt_pk_f16_f32 v34, v34, v37
	v_mul_f32_e32 v37, v36, v171
	v_or_b32_e32 v39, 0x30000, v130
	global_store_dword v39, v37, s[0:1]
	v_mul_f32_e32 v37, v38, v171
	v_or_b32_e32 v45, 0x16000, v130
	global_store_dword v39, v37, s[0:1] offset:128
	v_mul_f32_e32 v37, v41, v170
	v_or_b32_e32 v39, 0x32000, v130
	global_store_dword v45, v44, s[0:1]
	v_mul_f32_e32 v44, v43, v176
	global_store_dword v39, v37, s[0:1]
	v_exp_f32_e32 v37, v74
	v_mul_f32_e32 v43, v42, v170
	global_store_dword v39, v43, s[0:1] offset:128
	v_exp_f32_e32 v39, v58
	global_store_dword v45, v44, s[0:1] offset:128
	v_mul_f32_e32 v43, v37, v169
	v_or_b32_e32 v44, 0x34000, v130
	global_store_dword v44, v43, s[0:1]
	v_exp_f32_e32 v43, v75
	v_mul_f32_e32 v45, v39, v169
	global_store_dword v44, v45, s[0:1] offset:128
	v_exp_f32_e32 v44, v59
	v_mul_f32_e32 v45, v43, v168
	v_or_b32_e32 v46, 0x36000, v130
	global_store_dword v46, v45, s[0:1]
	v_mul_f32_e32 v45, v44, v168
	v_cvt_pk_f16_f32 v37, v37, v43
	v_cvt_pk_f16_f32 v36, v36, v41
	global_store_dword v46, v45, s[0:1] offset:128
	v_cvt_pk_f16_f32 v39, v39, v44
	v_cvt_pk_f16_f32 v38, v38, v42
	ds_write2_b64 v187, v[32:33], v[36:37] offset0:4 offset1:6
	ds_write2_b64 v40, v[34:35], v[38:39] offset0:36 offset1:38
	s_setprio 0
	ds_read_b64_tr_b16 v[32:33], v186
	ds_read_b64_tr_b16 v[34:35], v186 offset:288
	ds_read_b64_tr_b16 v[36:37], v185 offset:12288
	ds_read_b64_tr_b16 v[38:39], v185 offset:13056
	ds_read_b64_tr_b16 v[42:43], v185 offset:13120
	ds_read_b64_tr_b16 v[40:41], v185 offset:12352
	ds_read_b64_tr_b16 v[44:45], v186 offset:1152
	ds_read_b64_tr_b16 v[46:47], v186 offset:1440
	s_waitcnt lgkmcnt(4)
	v_mfma_f32_32x32x16_f16 v[0:15], v[32:35], v[36:39], v[0:15]
	s_waitcnt lgkmcnt(2)
	v_mfma_f32_32x32x16_f16 v[16:31], v[32:35], v[40:43], v[16:31]
	ds_read_b64_tr_b16 v[32:33], v185 offset:15360
	ds_read_b64_tr_b16 v[34:35], v185 offset:16128
	ds_read_b64_tr_b16 v[38:39], v185 offset:16192
	ds_read_b64_tr_b16 v[36:37], v185 offset:15424
	s_waitcnt lgkmcnt(2)
	v_mfma_f32_32x32x16_f16 v[0:15], v[44:47], v[32:35], v[0:15]
	s_waitcnt lgkmcnt(0)
	v_mfma_f32_32x32x16_f16 v[16:31], v[44:47], v[36:39], v[16:31]
	ds_read_b64_tr_b16 v[32:33], v186 offset:2304
	ds_read_b64_tr_b16 v[34:35], v186 offset:2592
	ds_read_b64_tr_b16 v[36:37], v185 offset:18432
	ds_read_b64_tr_b16 v[38:39], v185 offset:19200
	ds_read_b64_tr_b16 v[42:43], v185 offset:19264
	ds_read_b64_tr_b16 v[40:41], v185 offset:18496
	ds_read_b64_tr_b16 v[44:45], v186 offset:3456
	ds_read_b64_tr_b16 v[46:47], v186 offset:3744
	s_waitcnt lgkmcnt(4)
	v_mfma_f32_32x32x16_f16 v[0:15], v[32:35], v[36:39], v[0:15]
	s_waitcnt lgkmcnt(2)
	v_mfma_f32_32x32x16_f16 v[16:31], v[32:35], v[40:43], v[16:31]
	ds_read_b64_tr_b16 v[32:33], v185 offset:21504
	ds_read_b64_tr_b16 v[34:35], v185 offset:22272
	ds_read_b64_tr_b16 v[38:39], v185 offset:22336
	ds_read_b64_tr_b16 v[36:37], v185 offset:21568
	s_waitcnt lgkmcnt(2)
	v_mfma_f32_32x32x16_f16 v[0:15], v[44:47], v[32:35], v[0:15]
	s_waitcnt lgkmcnt(0)
	v_mfma_f32_32x32x16_f16 v[16:31], v[44:47], v[36:39], v[16:31]
	s_lshl_b32 s0, s2, 3
	s_and_b32 s0, s0, 0x7ffff800
	s_add_i32 s3, s3, s0
	s_lshl_b32 s0, s12, 7
	s_and_b32 s0, s0, 0x780
	s_add_u32 s0, s6, s0
	s_addc_u32 s1, s7, 0
	v_or_b32_e32 v32, s3, v184
	v_lshlrev_b32_e32 v34, 1, v164
	v_lshl_add_u32 v36, v32, 11, v34
	s_add_u32 s44, s0, 0x1000
	s_addc_u32 s45, s1, 0
	s_add_u32 s46, s44, 0x4000
	s_addc_u32 s47, s45, 0
	s_add_u32 s48, s46, 0x4000
	s_addc_u32 s49, s47, 0
	s_add_u32 s50, s48, 0x4000
	s_addc_u32 s51, s49, 0
	s_waitcnt vmcnt(63) expcnt(7) lgkmcnt(15)
	s_barrier
	v_fma_mixlo_f16 v38, v0, v183, 0
	global_store_short v36, v38, s[44:45] offset:-4096
	v_fma_mixlo_f16 v39, v16, v183, 0
	global_store_short v36, v39, s[44:45] offset:-4032
	v_fma_mixlo_f16 v40, v1, v182, 0
	global_store_short v36, v40, s[44:45] offset:-2048
	v_fma_mixlo_f16 v41, v17, v182, 0
	global_store_short v36, v41, s[44:45] offset:-1984
	v_fma_mixlo_f16 v38, v2, v181, 0
	global_store_short v36, v38, s[44:45]
	v_fma_mixlo_f16 v39, v18, v181, 0
	global_store_short v36, v39, s[44:45] offset:64
	v_fma_mixlo_f16 v40, v3, v180, 0
	global_store_short v36, v40, s[44:45] offset:2048
	v_fma_mixlo_f16 v41, v19, v180, 0
	global_store_short v36, v41, s[44:45] offset:2112
	v_fma_mixlo_f16 v38, v4, v179, 0
	global_store_short v36, v38, s[46:47] offset:-4096
	v_fma_mixlo_f16 v39, v20, v179, 0
	global_store_short v36, v39, s[46:47] offset:-4032
	v_fma_mixlo_f16 v40, v5, v178, 0
	global_store_short v36, v40, s[46:47] offset:-2048
	v_fma_mixlo_f16 v41, v21, v178, 0
	global_store_short v36, v41, s[46:47] offset:-1984
	v_fma_mixlo_f16 v38, v6, v177, 0
	global_store_short v36, v38, s[46:47]
	v_fma_mixlo_f16 v39, v22, v177, 0
	global_store_short v36, v39, s[46:47] offset:64
	v_fma_mixlo_f16 v40, v7, v176, 0
	global_store_short v36, v40, s[46:47] offset:2048
	v_fma_mixlo_f16 v41, v23, v176, 0
	global_store_short v36, v41, s[46:47] offset:2112
	v_fma_mixlo_f16 v38, v8, v175, 0
	global_store_short v36, v38, s[48:49] offset:-4096
	v_fma_mixlo_f16 v39, v24, v175, 0
	global_store_short v36, v39, s[48:49] offset:-4032
	v_fma_mixlo_f16 v40, v9, v174, 0
	global_store_short v36, v40, s[48:49] offset:-2048
	v_fma_mixlo_f16 v41, v25, v174, 0
	global_store_short v36, v41, s[48:49] offset:-1984
	v_fma_mixlo_f16 v38, v10, v173, 0
	global_store_short v36, v38, s[48:49]
	v_fma_mixlo_f16 v39, v26, v173, 0
	global_store_short v36, v39, s[48:49] offset:64
	v_fma_mixlo_f16 v40, v11, v172, 0
	global_store_short v36, v40, s[48:49] offset:2048
	v_fma_mixlo_f16 v41, v27, v172, 0
	global_store_short v36, v41, s[48:49] offset:2112
	v_fma_mixlo_f16 v38, v12, v171, 0
	global_store_short v36, v38, s[50:51] offset:-4096
	v_fma_mixlo_f16 v39, v28, v171, 0
	global_store_short v36, v39, s[50:51] offset:-4032
	v_fma_mixlo_f16 v40, v13, v170, 0
	global_store_short v36, v40, s[50:51] offset:-2048
	v_fma_mixlo_f16 v41, v29, v170, 0
	global_store_short v36, v41, s[50:51] offset:-1984
	v_fma_mixlo_f16 v38, v14, v169, 0
	global_store_short v36, v38, s[50:51]
	v_fma_mixlo_f16 v39, v30, v169, 0
	global_store_short v36, v39, s[50:51] offset:64
	v_fma_mixlo_f16 v40, v15, v168, 0
	global_store_short v36, v40, s[50:51] offset:2048
	v_fma_mixlo_f16 v41, v31, v168, 0
	global_store_short v36, v41, s[50:51] offset:2112
	s_endpgm
	.p2alignl 8, 3212836864
